# grid barrier: every arriver issues the acquire invalidate right behind its arrival atomic; the post-release invalidates are dropped (no cached loads are issued between arrival and release)
# baseline (speedup 1.0000x reference)
; __device__ __forceinline__ unsigned xb_add(unsigned* p, unsigned v) { unsigned GAS* g = (unsigned GAS*)p; asm volatile("" : "+s"(g)); return __hip_atomic_fetch_add(g, v, __ATOMIC_RELAXED, __HIP_MEMORY_SCOPE_AGENT); }
; __device__ __forceinline__ void xcd_barrier(const XcdBarrier& b) {
;     ...
;         unsigned nloc = b.st[0], nx = b.st[1];
;         if (nloc == 0u) { xcd_barrier_complete(bar, b.x, nloc, nx); b.st[0] = nloc; b.st[1] = nx; }
;         const unsigned old = xb_add(&bar[XB_XSUB(b.x)], 1u);
;         const unsigned gen = old / nloc;
;         if (old + 1u == (gen + 1u) * nloc) {
.LBB0_174:
	s_or_b64 exec, exec, s[10:11]
	buffer_inv sc1
	v_cvt_f32_u32_e32 v5, v3
	s_waitcnt vmcnt(1)
	v_readfirstlane_b32 s6, v4
	s_mov_b32 s30, 1
	v_rcp_iflag_f32_e32 v5, v5
	v_add_u32_e32 v6, s6, v2
	v_mul_f32_e32 v4, 0x4f7ffffe, v5
	v_cvt_u32_f32_e32 v4, v4
	v_sub_u32_e32 v5, 0, v3
	v_mul_lo_u32 v2, v5, v4
	v_mul_hi_u32 v2, v4, v2
	v_add_u32_e32 v2, v4, v2
	v_mul_hi_u32 v2, v6, v2
	v_mul_lo_u32 v4, v2, v3
	v_sub_u32_e32 v4, v6, v4
	v_add_u32_e32 v5, 1, v2
	v_cmp_ge_u32_e32 vcc, v4, v3
	s_nop 1
	v_cndmask_b32_e32 v2, v2, v5, vcc
	v_sub_u32_e32 v5, v4, v3
	v_cndmask_b32_e32 v4, v4, v5, vcc
	v_add_u32_e32 v5, 1, v2
	v_cmp_ge_u32_e32 vcc, v4, v3
	v_add_u32_e32 v4, 1, v6
	s_nop 0
	v_cndmask_b32_e32 v2, v2, v5, vcc
	v_mul_lo_u32 v5, v3, v2
	v_add_u32_e32 v3, v5, v3
	v_cmp_ne_u32_e32 vcc, v4, v3
	s_and_saveexec_b64 s[6:7], vcc
	s_xor_b64 s[6:7], exec, s[6:7]
	s_cbranch_execz .LBB0_190
	s_add_u32 s8, s4, 0x200
	s_addc_u32 s9, s5, 0
	s_add_u32 s10, s28, 0x2400
	s_addc_u32 s11, s29, 0
	s_mov_b64 s[12:13], 0
	s_waitcnt lgkmcnt(0)
	v_mov_b32_e32 v1, 0
	s_branch .LBB0_178

; __device__ __forceinline__ unsigned xb_ld(unsigned* p)              { unsigned GAS* g = (unsigned GAS*)p; asm volatile("" : "+s"(g)); return __hip_atomic_load(g, __ATOMIC_RELAXED, __HIP_MEMORY_SCOPE_AGENT); }
; __device__ __forceinline__ unsigned xb_add(unsigned* p, unsigned v) { unsigned GAS* g = (unsigned GAS*)p; asm volatile("" : "+s"(g)); return __hip_atomic_fetch_add(g, v, __ATOMIC_RELAXED, __HIP_MEMORY_SCOPE_AGENT); }
; #define XB_SPIN(cond, bar) do { unsigned _sp = 0; while (cond) { __builtin_amdgcn_s_sleep(1); \
;     if ((++_sp & 255u) == 0u) { if (xb_ld(&(bar)[XB_TMO])) break; if (_sp > XB_SPIN_CAP) { (void)xb_add(&(bar)[XB_TMO], 1u); break; } } } } while (0)
; __device__ __forceinline__ void xcd_barrier(const XcdBarrier& b) {
;     ...
;             __builtin_amdgcn_fence(__ATOMIC_RELEASE, "agent");
;             asm volatile("s_waitcnt vmcnt(0)" ::: "memory");
;             const unsigned og = xb_add(&bar[XB_TOP], 1u);
;             const unsigned tg = og / nx;
;             if (og + 1u == (tg + 1u) * nx) xb_add(&bar[XB_TOPGEN], 1u);
;             else XB_SPIN(xb_ld(&bar[XB_TOPGEN]) == tg, bar);
;             __builtin_amdgcn_fence(__ATOMIC_ACQUIRE, "agent");
;             xb_add(&bar[XB_XGEN(b.x)], 1u);
.LBB0_211:
	s_or_b64 exec, exec, s[4:5]
	s_mov_b64 s[6:7], exec
	v_mbcnt_lo_u32_b32 v1, s6, 0
	s_add_u32 s4, s28, 0x2400
	v_mbcnt_hi_u32_b32 v1, s7, v1
	s_addc_u32 s5, s29, 0
	v_cmp_eq_u32_e32 vcc, 0, v1
	s_waitcnt vmcnt(0)
	s_and_saveexec_b64 s[8:9], vcc
	s_cbranch_execz .LBB0_213
	s_bcnt1_i32_b64 s6, s[6:7]
	v_mov_b32_e32 v1, 0
	v_mov_b32_e32 v2, s6
	global_atomic_add v1, v2, s[4:5]

; __device__ __forceinline__ unsigned xb_add(unsigned* p, unsigned v) { unsigned GAS* g = (unsigned GAS*)p; asm volatile("" : "+s"(g)); return __hip_atomic_fetch_add(g, v, __ATOMIC_RELAXED, __HIP_MEMORY_SCOPE_AGENT); }
; __device__ __forceinline__ void xcd_barrier(const XcdBarrier& b) {
;     ...
;         unsigned nloc = b.st[0], nx = b.st[1];
;         if (nloc == 0u) { xcd_barrier_complete(bar, b.x, nloc, nx); b.st[0] = nloc; b.st[1] = nx; }
;         const unsigned old = xb_add(&bar[XB_XSUB(b.x)], 1u);
;         const unsigned gen = old / nloc;
;         if (old + 1u == (gen + 1u) * nloc) {
.LBB0_251:
	s_or_b64 exec, exec, s[8:9]
	buffer_inv sc1
	v_cvt_f32_u32_e32 v5, v3
	s_waitcnt vmcnt(1)
	v_readfirstlane_b32 s4, v4
	s_mov_b32 s28, 1
	v_rcp_iflag_f32_e32 v5, v5
	v_add_u32_e32 v6, s4, v2
	v_mul_f32_e32 v4, 0x4f7ffffe, v5
	v_cvt_u32_f32_e32 v4, v4
	v_sub_u32_e32 v5, 0, v3
	v_mul_lo_u32 v2, v5, v4
	v_mul_hi_u32 v2, v4, v2
	v_add_u32_e32 v2, v4, v2
	v_mul_hi_u32 v2, v6, v2
	v_mul_lo_u32 v4, v2, v3
	v_sub_u32_e32 v4, v6, v4
	v_add_u32_e32 v5, 1, v2
	v_cmp_ge_u32_e32 vcc, v4, v3
	s_nop 1
	v_cndmask_b32_e32 v2, v2, v5, vcc
	v_sub_u32_e32 v5, v4, v3
	v_cndmask_b32_e32 v4, v4, v5, vcc
	v_add_u32_e32 v5, 1, v2
	v_cmp_ge_u32_e32 vcc, v4, v3
	v_add_u32_e32 v4, 1, v6
	s_nop 0
	v_cndmask_b32_e32 v2, v2, v5, vcc
	v_mul_lo_u32 v5, v3, v2
	v_add_u32_e32 v3, v5, v3
	v_cmp_ne_u32_e32 vcc, v4, v3
	s_and_saveexec_b64 s[4:5], vcc
	s_xor_b64 s[4:5], exec, s[4:5]
	s_cbranch_execz .LBB0_267
	s_add_u32 s6, s2, 0x200
	s_addc_u32 s7, s3, 0
	s_add_u32 s8, s26, 0x2400
	s_addc_u32 s9, s27, 0
	s_mov_b64 s[10:11], 0
	s_waitcnt lgkmcnt(0)
	v_mov_b32_e32 v1, 0
	s_branch .LBB0_255

; __device__ __forceinline__ unsigned xb_ld(unsigned* p)              { unsigned GAS* g = (unsigned GAS*)p; asm volatile("" : "+s"(g)); return __hip_atomic_load(g, __ATOMIC_RELAXED, __HIP_MEMORY_SCOPE_AGENT); }
; __device__ __forceinline__ unsigned xb_add(unsigned* p, unsigned v) { unsigned GAS* g = (unsigned GAS*)p; asm volatile("" : "+s"(g)); return __hip_atomic_fetch_add(g, v, __ATOMIC_RELAXED, __HIP_MEMORY_SCOPE_AGENT); }
; #define XB_SPIN(cond, bar) do { unsigned _sp = 0; while (cond) { __builtin_amdgcn_s_sleep(1); \
;     if ((++_sp & 255u) == 0u) { if (xb_ld(&(bar)[XB_TMO])) break; if (_sp > XB_SPIN_CAP) { (void)xb_add(&(bar)[XB_TMO], 1u); break; } } } } while (0)
; __device__ __forceinline__ void xcd_barrier(const XcdBarrier& b) {
;     ...
;             __builtin_amdgcn_fence(__ATOMIC_RELEASE, "agent");
;             asm volatile("s_waitcnt vmcnt(0)" ::: "memory");
;             const unsigned og = xb_add(&bar[XB_TOP], 1u);
;             const unsigned tg = og / nx;
;             if (og + 1u == (tg + 1u) * nx) xb_add(&bar[XB_TOPGEN], 1u);
;             else XB_SPIN(xb_ld(&bar[XB_TOPGEN]) == tg, bar);
;             __builtin_amdgcn_fence(__ATOMIC_ACQUIRE, "agent");
;             xb_add(&bar[XB_XGEN(b.x)], 1u);
.LBB0_288:
	s_or_b64 exec, exec, s[2:3]
	s_mov_b64 s[4:5], exec
	v_mbcnt_lo_u32_b32 v1, s4, 0
	s_add_u32 s2, s26, 0x2400
	v_mbcnt_hi_u32_b32 v1, s5, v1
	s_addc_u32 s3, s27, 0
	v_cmp_eq_u32_e32 vcc, 0, v1
	s_waitcnt vmcnt(0)
	s_and_saveexec_b64 s[6:7], vcc
	s_cbranch_execz .LBB0_290
	s_bcnt1_i32_b64 s4, s[4:5]
	v_mov_b32_e32 v1, 0
	v_mov_b32_e32 v2, s4
	global_atomic_add v1, v2, s[2:3]

; __device__ __forceinline__ unsigned xb_add(unsigned* p, unsigned v) { unsigned GAS* g = (unsigned GAS*)p; asm volatile("" : "+s"(g)); return __hip_atomic_fetch_add(g, v, __ATOMIC_RELAXED, __HIP_MEMORY_SCOPE_AGENT); }
; __device__ __forceinline__ void xcd_barrier(const XcdBarrier& b) {
;     ...
;         unsigned nloc = b.st[0], nx = b.st[1];
;         if (nloc == 0u) { xcd_barrier_complete(bar, b.x, nloc, nx); b.st[0] = nloc; b.st[1] = nx; }
;         const unsigned old = xb_add(&bar[XB_XSUB(b.x)], 1u);
;         const unsigned gen = old / nloc;
;         if (old + 1u == (gen + 1u) * nloc) {
.LBB0_447:
	s_or_b64 exec, exec, s[8:9]
	buffer_inv sc1
	v_cvt_f32_u32_e32 v6, v4
	s_waitcnt vmcnt(1)
	v_readfirstlane_b32 s4, v5
	v_sub_u32_e32 v5, 0, v4
	v_rcp_iflag_f32_e32 v6, v6
	v_add_u32_e32 v7, s4, v2
	v_mul_f32_e32 v6, 0x4f7ffffe, v6
	v_cvt_u32_f32_e32 v6, v6
	v_mul_lo_u32 v2, v5, v6
	v_mul_hi_u32 v2, v6, v2
	v_add_u32_e32 v2, v6, v2
	v_mul_hi_u32 v2, v7, v2
	v_mul_lo_u32 v5, v2, v4
	v_sub_u32_e32 v5, v7, v5
	v_add_u32_e32 v6, 1, v2
	v_cmp_ge_u32_e32 vcc, v5, v4
	s_nop 1
	v_cndmask_b32_e32 v2, v2, v6, vcc
	v_sub_u32_e32 v6, v5, v4
	v_cndmask_b32_e32 v5, v5, v6, vcc
	v_add_u32_e32 v6, 1, v2
	v_cmp_ge_u32_e32 vcc, v5, v4
	v_add_u32_e32 v5, 1, v7
	s_nop 0
	v_cndmask_b32_e32 v2, v2, v6, vcc
	v_mul_lo_u32 v6, v4, v2
	v_add_u32_e32 v4, v6, v4
	v_cmp_ne_u32_e32 vcc, v5, v4
	s_and_saveexec_b64 s[4:5], vcc
	s_xor_b64 s[4:5], exec, s[4:5]
	s_cbranch_execz .LBB0_463
	s_add_u32 s6, s2, 0x200
	s_addc_u32 s7, s3, 0
	s_add_u32 s8, s27, 0x2400
	s_addc_u32 s9, s28, 0
	s_mov_b32 s29, 1
	s_mov_b64 s[10:11], 0
	s_branch .LBB0_451

; __device__ __forceinline__ unsigned xb_ld(unsigned* p)              { unsigned GAS* g = (unsigned GAS*)p; asm volatile("" : "+s"(g)); return __hip_atomic_load(g, __ATOMIC_RELAXED, __HIP_MEMORY_SCOPE_AGENT); }
; __device__ __forceinline__ unsigned xb_add(unsigned* p, unsigned v) { unsigned GAS* g = (unsigned GAS*)p; asm volatile("" : "+s"(g)); return __hip_atomic_fetch_add(g, v, __ATOMIC_RELAXED, __HIP_MEMORY_SCOPE_AGENT); }
; #define XB_SPIN(cond, bar) do { unsigned _sp = 0; while (cond) { __builtin_amdgcn_s_sleep(1); \
;     if ((++_sp & 255u) == 0u) { if (xb_ld(&(bar)[XB_TMO])) break; if (_sp > XB_SPIN_CAP) { (void)xb_add(&(bar)[XB_TMO], 1u); break; } } } } while (0)
; __device__ __forceinline__ void xcd_barrier(const XcdBarrier& b) {
;     ...
;             __builtin_amdgcn_fence(__ATOMIC_RELEASE, "agent");
;             asm volatile("s_waitcnt vmcnt(0)" ::: "memory");
;             const unsigned og = xb_add(&bar[XB_TOP], 1u);
;             const unsigned tg = og / nx;
;             if (og + 1u == (tg + 1u) * nx) xb_add(&bar[XB_TOPGEN], 1u);
;             else XB_SPIN(xb_ld(&bar[XB_TOPGEN]) == tg, bar);
;             __builtin_amdgcn_fence(__ATOMIC_ACQUIRE, "agent");
;             xb_add(&bar[XB_XGEN(b.x)], 1u);
.LBB0_484:
	s_or_b64 exec, exec, s[2:3]
	s_mov_b64 s[4:5], exec
	v_mbcnt_lo_u32_b32 v2, s4, 0
	s_add_u32 s2, s27, 0x2400
	v_mbcnt_hi_u32_b32 v2, s5, v2
	s_addc_u32 s3, s28, 0
	v_cmp_eq_u32_e32 vcc, 0, v2
	s_waitcnt vmcnt(0)
	s_and_saveexec_b64 s[6:7], vcc
	s_cbranch_execz .LBB0_486
	s_bcnt1_i32_b64 s4, s[4:5]
	v_mov_b32_e32 v2, s4
	global_atomic_add v35, v2, s[2:3]

; __device__ __forceinline__ unsigned xb_add(unsigned* p, unsigned v) { unsigned GAS* g = (unsigned GAS*)p; asm volatile("" : "+s"(g)); return __hip_atomic_fetch_add(g, v, __ATOMIC_RELAXED, __HIP_MEMORY_SCOPE_AGENT); }
; __device__ __forceinline__ void xcd_barrier(const XcdBarrier& b) {
;     ...
;         unsigned nloc = b.st[0], nx = b.st[1];
;         if (nloc == 0u) { xcd_barrier_complete(bar, b.x, nloc, nx); b.st[0] = nloc; b.st[1] = nx; }
;         const unsigned old = xb_add(&bar[XB_XSUB(b.x)], 1u);
;         const unsigned gen = old / nloc;
;         if (old + 1u == (gen + 1u) * nloc) {
.LBB0_1444:
	s_or_b64 exec, exec, s[10:11]
	buffer_inv sc1
	v_cvt_f32_u32_e32 v6, v4
	s_waitcnt vmcnt(1)
	v_readfirstlane_b32 s4, v5
	v_sub_u32_e32 v5, 0, v4
	v_rcp_iflag_f32_e32 v6, v6
	v_add_u32_e32 v7, s4, v2
	v_mul_f32_e32 v6, 0x4f7ffffe, v6
	v_cvt_u32_f32_e32 v6, v6
	v_mul_lo_u32 v2, v5, v6
	v_mul_hi_u32 v2, v6, v2
	v_add_u32_e32 v2, v6, v2
	v_mul_hi_u32 v2, v7, v2
	v_mul_lo_u32 v5, v2, v4
	v_sub_u32_e32 v5, v7, v5
	v_add_u32_e32 v6, 1, v2
	v_cmp_ge_u32_e32 vcc, v5, v4
	s_nop 1
	v_cndmask_b32_e32 v2, v2, v6, vcc
	v_sub_u32_e32 v6, v5, v4
	v_cndmask_b32_e32 v5, v5, v6, vcc
	v_add_u32_e32 v6, 1, v2
	v_cmp_ge_u32_e32 vcc, v5, v4
	v_add_u32_e32 v5, 1, v7
	s_nop 0
	v_cndmask_b32_e32 v2, v2, v6, vcc
	v_mul_lo_u32 v6, v4, v2
	v_add_u32_e32 v4, v6, v4
	v_cmp_ne_u32_e32 vcc, v5, v4
	s_and_saveexec_b64 s[4:5], vcc
	s_xor_b64 s[4:5], exec, s[4:5]
	s_cbranch_execz .LBB0_1460
	s_add_u32 s6, s2, 0x200
	s_addc_u32 s7, s3, 0
	s_add_u32 s10, s29, 0x2400
	s_addc_u32 s11, s30, 0
	s_mov_b32 s31, 1
	s_mov_b64 s[12:13], 0
	s_branch .LBB0_1448

; __device__ __forceinline__ unsigned xb_ld(unsigned* p)              { unsigned GAS* g = (unsigned GAS*)p; asm volatile("" : "+s"(g)); return __hip_atomic_load(g, __ATOMIC_RELAXED, __HIP_MEMORY_SCOPE_AGENT); }
; __device__ __forceinline__ unsigned xb_add(unsigned* p, unsigned v) { unsigned GAS* g = (unsigned GAS*)p; asm volatile("" : "+s"(g)); return __hip_atomic_fetch_add(g, v, __ATOMIC_RELAXED, __HIP_MEMORY_SCOPE_AGENT); }
; #define XB_SPIN(cond, bar) do { unsigned _sp = 0; while (cond) { __builtin_amdgcn_s_sleep(1); \
;     if ((++_sp & 255u) == 0u) { if (xb_ld(&(bar)[XB_TMO])) break; if (_sp > XB_SPIN_CAP) { (void)xb_add(&(bar)[XB_TMO], 1u); break; } } } } while (0)
; __device__ __forceinline__ void xcd_barrier(const XcdBarrier& b) {
;     ...
;             __builtin_amdgcn_fence(__ATOMIC_RELEASE, "agent");
;             asm volatile("s_waitcnt vmcnt(0)" ::: "memory");
;             const unsigned og = xb_add(&bar[XB_TOP], 1u);
;             const unsigned tg = og / nx;
;             if (og + 1u == (tg + 1u) * nx) xb_add(&bar[XB_TOPGEN], 1u);
;             else XB_SPIN(xb_ld(&bar[XB_TOPGEN]) == tg, bar);
;             __builtin_amdgcn_fence(__ATOMIC_ACQUIRE, "agent");
;             xb_add(&bar[XB_XGEN(b.x)], 1u);
.LBB0_1481:
	s_or_b64 exec, exec, s[2:3]
	s_mov_b64 s[4:5], exec
	v_mbcnt_lo_u32_b32 v2, s4, 0
	s_add_u32 s2, s29, 0x2400
	v_mbcnt_hi_u32_b32 v2, s5, v2
	s_addc_u32 s3, s30, 0
	v_cmp_eq_u32_e32 vcc, 0, v2
	s_waitcnt vmcnt(0)
	s_and_saveexec_b64 s[6:7], vcc
	s_cbranch_execz .LBB0_1483
	s_bcnt1_i32_b64 s4, s[4:5]
	v_mov_b32_e32 v2, s4
	global_atomic_add v35, v2, s[2:3]

; __device__ __forceinline__ unsigned xb_add(unsigned* p, unsigned v) { unsigned GAS* g = (unsigned GAS*)p; asm volatile("" : "+s"(g)); return __hip_atomic_fetch_add(g, v, __ATOMIC_RELAXED, __HIP_MEMORY_SCOPE_AGENT); }
; __device__ __forceinline__ void xcd_barrier(const XcdBarrier& b) {
;     ...
;         unsigned nloc = b.st[0], nx = b.st[1];
;         if (nloc == 0u) { xcd_barrier_complete(bar, b.x, nloc, nx); b.st[0] = nloc; b.st[1] = nx; }
;         const unsigned old = xb_add(&bar[XB_XSUB(b.x)], 1u);
;         const unsigned gen = old / nloc;
;         if (old + 1u == (gen + 1u) * nloc) {
.LBB0_1537:
	s_or_b64 exec, exec, s[8:9]
	buffer_inv sc1
	v_cvt_f32_u32_e32 v6, v4
	s_waitcnt vmcnt(1)
	v_readfirstlane_b32 s4, v5
	v_sub_u32_e32 v5, 0, v4
	v_rcp_iflag_f32_e32 v6, v6
	v_add_u32_e32 v7, s4, v2
	v_mul_f32_e32 v6, 0x4f7ffffe, v6
	v_cvt_u32_f32_e32 v6, v6
	v_mul_lo_u32 v2, v5, v6
	v_mul_hi_u32 v2, v6, v2
	v_add_u32_e32 v2, v6, v2
	v_mul_hi_u32 v2, v7, v2
	v_mul_lo_u32 v5, v2, v4
	v_sub_u32_e32 v5, v7, v5
	v_add_u32_e32 v6, 1, v2
	v_cmp_ge_u32_e32 vcc, v5, v4
	s_nop 1
	v_cndmask_b32_e32 v2, v2, v6, vcc
	v_sub_u32_e32 v6, v5, v4
	v_cndmask_b32_e32 v5, v5, v6, vcc
	v_add_u32_e32 v6, 1, v2
	v_cmp_ge_u32_e32 vcc, v5, v4
	v_add_u32_e32 v5, 1, v7
	s_nop 0
	v_cndmask_b32_e32 v2, v2, v6, vcc
	v_mul_lo_u32 v6, v4, v2
	v_add_u32_e32 v4, v6, v4
	v_cmp_ne_u32_e32 vcc, v5, v4
	s_and_saveexec_b64 s[4:5], vcc
	s_xor_b64 s[4:5], exec, s[4:5]
	s_cbranch_execz .LBB0_1553
	s_add_u32 s6, s2, 0x200
	s_addc_u32 s7, s3, 0
	s_add_u32 s8, s26, 0x2400
	s_addc_u32 s9, s27, 0
	s_mov_b32 s28, 1
	s_mov_b64 s[10:11], 0
	s_branch .LBB0_1541

; __device__ __forceinline__ unsigned xb_ld(unsigned* p)              { unsigned GAS* g = (unsigned GAS*)p; asm volatile("" : "+s"(g)); return __hip_atomic_load(g, __ATOMIC_RELAXED, __HIP_MEMORY_SCOPE_AGENT); }
; __device__ __forceinline__ unsigned xb_add(unsigned* p, unsigned v) { unsigned GAS* g = (unsigned GAS*)p; asm volatile("" : "+s"(g)); return __hip_atomic_fetch_add(g, v, __ATOMIC_RELAXED, __HIP_MEMORY_SCOPE_AGENT); }
; #define XB_SPIN(cond, bar) do { unsigned _sp = 0; while (cond) { __builtin_amdgcn_s_sleep(1); \
;     if ((++_sp & 255u) == 0u) { if (xb_ld(&(bar)[XB_TMO])) break; if (_sp > XB_SPIN_CAP) { (void)xb_add(&(bar)[XB_TMO], 1u); break; } } } } while (0)
; __device__ __forceinline__ void xcd_barrier(const XcdBarrier& b) {
;     ...
;             __builtin_amdgcn_fence(__ATOMIC_RELEASE, "agent");
;             asm volatile("s_waitcnt vmcnt(0)" ::: "memory");
;             const unsigned og = xb_add(&bar[XB_TOP], 1u);
;             const unsigned tg = og / nx;
;             if (og + 1u == (tg + 1u) * nx) xb_add(&bar[XB_TOPGEN], 1u);
;             else XB_SPIN(xb_ld(&bar[XB_TOPGEN]) == tg, bar);
;             __builtin_amdgcn_fence(__ATOMIC_ACQUIRE, "agent");
;             xb_add(&bar[XB_XGEN(b.x)], 1u);
.LBB0_1574:
	s_or_b64 exec, exec, s[2:3]
	s_mov_b64 s[4:5], exec
	v_mbcnt_lo_u32_b32 v2, s4, 0
	s_add_u32 s2, s26, 0x2400
	v_mbcnt_hi_u32_b32 v2, s5, v2
	s_addc_u32 s3, s27, 0
	v_cmp_eq_u32_e32 vcc, 0, v2
	s_waitcnt vmcnt(0)
	s_and_saveexec_b64 s[6:7], vcc
	s_cbranch_execnz .LBB0_1575
	s_getpc_b64 s[98:99]
